# attn: key-tile rotation (2qb+13head)&31
# speedup vs baseline: 1.0610x; 1.0051x over previous
.Lp_top:
	s_lshl_b32 s6, s21, 20
	s_add_u32 s4, s4, s6
	s_addc_u32 s5, s5, 0
	v_lshlrev_b32_e32 v54, 4, v0
	v_mov_b32_e32 v55, v63
	s_lshl_b32 s3, s3, 1
	s_mul_i32 s20, s21, 13
	v_lshl_add_u64 v[4:5], s[4:5], 0, v[54:55]
	s_mov_b64 s[4:5], 0x1000000
	s_add_i32 s20, s20, s3
	v_lshl_add_u64 v[170:171], v[4:5], 0, s[4:5]
	s_and_b32 s22, s20, 31
	s_lshl_b32 s4, s20, 12
	s_lshl_b32 s12, s22, 13
	s_add_i32 s5, s4, 0x1000
	v_lshl_add_u64 v[58:59], v[170:171], 0, s[12:13]
	s_mov_b32 s3, 0x80000
	s_and_b32 s5, s5, 0x1f000
	v_add_co_u32_e32 v16, vcc, s3, v58
	s_lshl_b32 s12, s5, 1
	s_nop 0
	v_addc_co_u32_e32 v17, vcc, 0, v59, vcc
	v_lshl_add_u64 v[56:57], v[170:171], 0, s[12:13]
	global_load_dwordx4 v[4:7], v[58:59], off
	global_load_dwordx4 v[8:11], v[56:57], off
	global_load_dwordx4 v[12:15], v[16:17], off
	v_add_co_u32_e32 v16, vcc, s3, v56
	v_lshrrev_b32_e32 v184, 8, v0
	s_nop 0
	v_addc_co_u32_e32 v17, vcc, 0, v57, vcc
	global_load_dwordx4 v[16:19], v[16:17], off
	v_and_b32_e32 v20, 19, v0
	v_lshlrev_b32_e32 v21, 1, v0
	v_and_b32_e32 v2, 4, v2
	v_and_or_b32 v20, v21, 8, v20
	v_lshlrev_b32_e32 v101, 5, v184
	s_addk_i32 s4, 0x2000
	v_or3_b32 v2, v20, v2, v101
	s_and_b32 s4, s4, 0x1f000
	v_mul_u32_u24_e32 v2, 0x48, v2
	s_lshl_b32 s12, s4, 1
	v_lshlrev_b32_e32 v3, 3, v0
	v_lshlrev_b32_e32 v100, 1, v99
	v_lshlrev_b32_e32 v2, 1, v2
	v_lshl_add_u64 v[60:61], v[170:171], 0, s[12:13]
	v_and_b32_e32 v3, 56, v3
	v_add3_u32 v186, 0, v2, v100
	v_add_co_u32_e32 v2, vcc, s3, v60
	v_lshlrev_b32_e32 v68, 1, v3
	s_nop 0
	v_addc_co_u32_e32 v3, vcc, 0, v61, vcc
	global_load_dwordx4 v[162:165], v[60:61], off
	global_load_dwordx4 v[166:169], v[2:3], off
	v_lshrrev_b32_e32 v82, 3, v0
	v_mul_u32_u24_e32 v22, 0x48, v82
	v_lshlrev_b32_e32 v21, 1, v22
	v_add3_u32 v185, 0, v21, v68
	s_mov_b64 s[24:25], 0x80000
	s_add_i32 s17, s20, 3
	s_add_i32 s18, s20, 4
	v_mov_b32_e32 v62, v63
	v_lshrrev_b32_e32 v55, 6, v0
	v_mov_b32_e32 v83, 0
	v_mov_b32_e32 v84, 0
	v_lshl_add_u64 v[70:71], v[58:59], 0, s[24:25]
	v_lshl_add_u64 v[66:67], v[56:57], 0, s[24:25]
	v_lshl_add_u64 v[64:65], v[60:61], 0, s[24:25]
	s_waitcnt vmcnt(5)
	ds_write_b128 v185, v[4:7]
	s_waitcnt vmcnt(3)
	ds_write_b128 v185, v[12:15] offset:9216
	ds_write_b128 v185, v[8:11] offset:18432
	s_waitcnt vmcnt(2)
	ds_write_b128 v185, v[16:19] offset:27648
	s_waitcnt lgkmcnt(0)
	s_barrier
	ds_read_b128 v[2:5], v186
	ds_read_b128 v[38:41], v186 offset:32
	s_waitcnt lgkmcnt(1)
	v_mfma_f32_32x32x16_f16 v[2:17], v[2:5], v[114:117], 0
	ds_read_b128 v[18:21], v186 offset:9216
	ds_read_b128 v[46:49], v186 offset:9248
	s_waitcnt lgkmcnt(1)
	v_mfma_f32_32x32x16_f16 v[18:33], v[18:21], v[130:133], 0
	v_mfma_f32_32x32x16_f16 v[2:17], v[38:41], v[118:121], v[2:17]
	s_waitcnt lgkmcnt(0)
	v_mfma_f32_32x32x16_f16 v[18:33], v[46:49], v[134:137], v[18:33]
	ds_read_b128 v[38:41], v186 offset:64
	ds_read_b128 v[46:49], v186 offset:96
	s_waitcnt lgkmcnt(1)
	v_mfma_f32_32x32x16_f16 v[2:17], v[38:41], v[122:125], v[2:17]
	ds_read_b128 v[38:41], v186 offset:9280
	ds_read_b128 v[50:53], v186 offset:9312
	s_load_dwordx4 s[4:7], s[0:1], 0x38
	s_load_dwordx2 s[14:15], s[0:1], 0x8
	s_mov_b32 s0, -2
	s_mov_b32 s1, 0x3f800000
	s_waitcnt lgkmcnt(0)
	s_barrier
	v_mfma_f32_32x32x16_f16 v[18:33], v[38:41], v[138:141], v[18:33]
	v_mfma_f32_32x32x16_f16 v[2:17], v[46:49], v[126:129], v[2:17]
	v_mfma_f32_32x32x16_f16 v[18:33], v[50:53], v[142:145], v[18:33]
	s_lshl_b32 s12, s17, 13
	s_and_b32 s12, s12, 0x3e000
	s_add_u32 s28, s12, s3
	s_mov_b32 s29, 0
	v_lshl_add_u64 v[176:177], v[170:171], 0, s[12:13]
	global_load_dwordx4 v[50:53], v[176:177], off
	v_lshl_add_u64 v[176:177], v[170:171], 0, s[28:29]
	global_load_dwordx4 v[94:97], v[176:177], off
	s_nop 7
	s_cmp_eq_u32 s37, 1
	s_cbranch_scc0 .Lf_A
	v_mov_b32_e32 v83, 0xf149f2ca
	v_mov_b32_e32 v84, 0xf149f2ca
	s_branch .Ls_A

.Ll1_cont:
	ds_bpermute_b32 v2, v69, v84
	ds_bpermute_b32 v5, v69, v83
	v_max_f32_e32 v4, v84, v84
	v_max_f32_e32 v7, v83, v83
	ds_bpermute_b32 v3, v69, v63
	s_waitcnt lgkmcnt(2)
	v_max_f32_e32 v6, v2, v2
	v_max_f32_e32 v4, v4, v6
	v_sub_f32_e32 v6, v84, v4
	v_exp_f32_e32 v9, v6
	s_waitcnt lgkmcnt(1)
	v_max_f32_e32 v6, v5, v5
	v_sub_f32_e32 v2, v2, v4
	v_max_f32_e32 v6, v7, v6
	v_exp_f32_e32 v11, v2
	ds_bpermute_b32 v2, v69, v62
	v_sub_f32_e32 v5, v5, v6
	v_sub_f32_e32 v7, v83, v6
	v_exp_f32_e32 v10, v5
	v_exp_f32_e32 v8, v7
	v_cmp_gt_u32_e32 vcc, 32, v98
	s_waitcnt lgkmcnt(0)
	v_pk_mul_f32 v[2:3], v[10:11], v[2:3]
	s_nop 0
	v_pk_fma_f32 v[8:9], v[62:63], v[8:9], v[2:3]
	v_lshlrev_b32_e32 v2, 7, v184
	v_or3_b32 v10, v183, v2, v1
	s_and_saveexec_b64 s[0:1], vcc
	v_lshl_add_u32 v2, v10, 4, 0
	v_add_u32_e32 v2, 0x21000, v2
	v_mov_b32_e32 v5, v9
	v_mov_b32_e32 v7, v8
	ds_write_b128 v2, v[4:7]
	s_or_b64 exec, exec, s[0:1]
	s_lshl_b32 s12, s21, 7
	s_mov_b32 s3, 0
	v_or_b32_e32 v2, s12, v82
	s_lshl_b32 s13, s21, 11
	s_add_i32 s23, 0, 0x12000
	v_lshlrev_b32_e32 v2, 12, v2
	v_mov_b32_e32 v3, 0
	s_add_i32 s13, s13, s16
	s_lshl_b64 s[0:1], s[2:3], 13
	v_lshl_add_u64 v[12:13], s[14:15], 0, v[2:3]
	v_mov_b32_e32 v69, v3
	s_add_u32 s0, s10, s0
	v_lshl_add_u64 v[172:173], v[12:13], 0, v[68:69]
	s_addc_u32 s1, s11, s1
	s_lshl_b32 s10, s22, 7
	s_mov_b32 s11, s3
	s_waitcnt vmcnt(1)
	v_lshl_add_u64 v[36:37], v[172:173], 0, s[10:11]
	s_mov_b32 s10, 0x40000
	v_add_co_u32_e32 v38, vcc, s10, v36
	s_waitcnt lgkmcnt(0)
	s_barrier
	global_load_dwordx4 v[12:15], v[58:59], off
	global_load_dwordx4 v[16:19], v[70:71], off
	v_addc_co_u32_e32 v39, vcc, 0, v37, vcc
	global_load_dwordx4 v[20:23], v[56:57], off
	global_load_dwordx4 v[24:27], v[66:67], off
	global_load_dwordx4 v[28:31], v[36:37], off
	global_load_dwordx4 v[32:35], v[38:39], off
	v_add_f32_e32 v2, v78, v80
	s_movk_i32 s11, 0x1200
	v_add_f32_e32 v5, v79, v81
	s_mov_b32 s14, 0x3fb8aa3b
	v_lshlrev_b32_e32 v10, 4, v10
	v_mov_b32_e32 v36, s23
	v_mul_f32_e32 v37, 0x3fb8aa3b, v2
	v_mul_f32_e32 v38, 0x3fb8aa3b, v5
	v_xor_b32_e32 v10, 0x800, v10
	v_mad_u32_u24 v40, v55, s11, v36
	v_fma_f32 v36, v2, s14, -v37
	v_rndne_f32_e32 v39, v37
	v_fma_f32 v41, v5, s14, -v38
	s_waitcnt vmcnt(6)
	v_rndne_f32_e32 v42, v38
	v_add_u32_e32 v10, 0, v10
	v_fmac_f32_e32 v36, 0x32a5705f, v2
	v_sub_f32_e32 v37, v37, v39
	v_fmac_f32_e32 v41, 0x32a5705f, v5
	v_sub_f32_e32 v38, v38, v42
	v_add_u32_e32 v10, 0x21000, v10
	v_add_f32_e32 v44, v37, v36
	global_load_dwordx4 v[146:149], v[60:61], off
	global_load_dwordx4 v[150:153], v[64:65], off
	v_cvt_i32_f32_e32 v43, v39
	v_add_f32_e32 v41, v38, v41
	ds_read_b128 v[36:39], v10
	v_exp_f32_e32 v10, v44
	v_cvt_i32_f32_e32 v42, v42
	v_exp_f32_e32 v41, v41
	s_mov_b32 s21, 0xc2ce8ed0
	s_lshl_b32 s11, s20, 6
	s_add_i32 s14, s11, 64
	v_ldexp_f32 v10, v10, v43
	v_cmp_ngt_f32_e32 vcc, s21, v2
	s_mov_b32 s22, 0x42b17218
	s_and_b32 s14, s14, 0x7c0
	v_ldexp_f32 v41, v41, v42
	v_cndmask_b32_e32 v10, 0, v10, vcc
	v_cmp_ngt_f32_e32 vcc, s21, v5
	v_mov_b32_e32 v7, 0x7f800000
	v_max_f32_e32 v11, v4, v4
	s_mov_b32 s15, s3
	s_lshl_b32 s14, s14, 1
	s_waitcnt lgkmcnt(0)
	v_max_f32_e32 v42, v36, v36
	v_cndmask_b32_e32 v41, 0, v41, vcc
	v_cmp_nlt_f32_e32 vcc, s22, v2
	v_max_f32_e32 v187, v11, v42
	v_mov_b32_e32 v55, v3
	v_cndmask_b32_e32 v2, v7, v10, vcc
	v_cmp_nlt_f32_e32 vcc, s22, v5
	v_lshl_add_u64 v[10:11], v[172:173], 0, s[14:15]
	v_lshl_add_u64 v[178:179], s[0:1], 0, v[54:55]
	v_cndmask_b32_e32 v5, v7, v41, vcc
	v_sub_f32_e32 v2, v2, v5
	v_add_f32_e32 v41, 0x3e4ccccd, v2
	v_sub_f32_e32 v2, v4, v187
	v_max_f32_e32 v4, v6, v6
	s_and_b32 s1, s2, 7
	s_mulk_i32 s1, 0x680
	s_mulk_i32 s19, 0x340
	s_add_i32 s0, s20, 2
	s_waitcnt vmcnt(7)
	ds_write_b128 v185, v[12:15]
	s_waitcnt vmcnt(6)
	ds_write_b128 v185, v[16:19] offset:9216
	s_waitcnt vmcnt(5)
	ds_write_b128 v185, v[20:23] offset:18432
	s_waitcnt vmcnt(4)
	ds_write_b128 v185, v[24:27] offset:27648
	s_waitcnt vmcnt(3)
	ds_write_b128 v185, v[28:31] offset:36864
	s_waitcnt vmcnt(2)
	ds_write_b128 v185, v[32:35] offset:46080
	v_add_co_u32_e32 v12, vcc, s10, v10
	v_exp_f32_e32 v23, v2
	s_nop 0
	v_addc_co_u32_e32 v13, vcc, 0, v11, vcc
	global_load_dwordx4 v[154:157], v[10:11], off
	global_load_dwordx4 v[158:161], v[12:13], off
	s_waitcnt lgkmcnt(0)
	s_barrier
	ds_read_b128 v[10:13], v186
	v_sub_f32_e32 v2, v36, v187
	v_exp_f32_e32 v25, v2
	v_max_f32_e32 v2, v38, v38
	v_max_f32_e32 v188, v4, v2
	v_sub_f32_e32 v2, v6, v188
	v_exp_f32_e32 v22, v2
	v_sub_f32_e32 v2, v38, v188
	v_exp_f32_e32 v24, v2
	ds_read_b128 v[14:17], v186 offset:9216
	ds_read_b128 v[18:21], v186 offset:32
	s_waitcnt lgkmcnt(2)
	v_mfma_f32_32x32x16_f16 v[66:81], v[10:13], v[114:117], 0
	v_mov_b32_e32 v36, v39
	v_mul_f32_e64 v10, v36, v24
	v_mul_f32_e64 v11, v37, v25
	ds_read_b128 v[4:7], v186 offset:9248
	s_add_i32 s1, s1, s19
	s_mov_b32 s14, 0x30000
	s_mov_b32 s15, 0x80000
	s_mov_b32 s19, 0
	s_waitcnt lgkmcnt(2)
	v_mfma_f32_32x32x16_f16 v[82:97], v[14:17], v[130:133], 0
	v_fma_f32 v16, v8, v22, v10
	v_fma_f32 v17, v9, v23, v11
	v_log_f32_e32 v238, v17
	s_nop 0
	v_add_f32_e32 v187, v187, v238
	v_sub_f32_e32 v240, 0, v187
	v_sub_f32_e32 v241, 0, v187
	v_sub_f32_e32 v242, 0, v187
	v_sub_f32_e32 v243, 0, v187
	v_sub_f32_e32 v244, 0, v187
	v_sub_f32_e32 v245, 0, v187
	v_sub_f32_e32 v246, 0, v187
	v_sub_f32_e32 v247, 0, v187
	v_sub_f32_e32 v248, 0, v187
	v_sub_f32_e32 v249, 0, v187
	v_sub_f32_e32 v250, 0, v187
	v_sub_f32_e32 v251, 0, v187
	v_sub_f32_e32 v252, 0, v187
	v_sub_f32_e32 v253, 0, v187
	v_sub_f32_e32 v254, 0, v187
	v_sub_f32_e32 v255, 0, v187
	v_lshrrev_b32_e32 v22, 3, v98
	v_or3_b32 v2, s13, v183, v22
	v_lshlrev_b64 v[8:9], 13, v[2:3]
	v_lshl_add_u64 v[8:9], s[4:5], 0, v[8:9]
	v_lshlrev_b32_e32 v2, 2, v101
	v_lshl_add_u64 v[8:9], v[8:9], 0, v[2:3]
	v_and_b32_e32 v2, 0x70, v54
	v_lshl_add_u64 v[174:175], v[8:9], 0, v[2:3]
	ds_read_b128 v[8:11], v186 offset:64
	s_waitcnt lgkmcnt(2)
	v_mfma_f32_32x32x16_f16 v[66:81], v[18:21], v[118:121], v[66:81]
	v_div_scale_f32 v18, s[4:5], v16, v16, -v41
	v_rcp_f32_e32 v19, v18
	v_div_scale_f32 v20, vcc, -v41, v16, -v41
	s_mov_b32 s13, 0x20000
	v_mov_b32_e32 v24, v3
	s_waitcnt lgkmcnt(1)
	v_mfma_f32_32x32x16_f16 v[82:97], v[4:7], v[134:137], v[82:97]
	v_fma_f32 v4, -v18, v19, 1.0
	v_fmac_f32_e32 v19, v4, v19
	v_mul_f32_e32 v21, v20, v19
	ds_read_b128 v[4:7], v186 offset:9280
	ds_read_b128 v[12:15], v186 offset:96
	v_mov_b32_e32 v25, v3
	v_mov_b32_e32 v26, v3
	v_mov_b32_e32 v27, v3
	s_waitcnt lgkmcnt(2)
	v_mfma_f32_32x32x16_f16 v[66:81], v[8:11], v[122:125], v[66:81]
	v_fma_f32 v8, -v18, v21, v20
	v_fmac_f32_e32 v21, v8, v19
	v_fma_f32 v18, -v18, v21, v20
	v_div_scale_f32 v20, s[4:5], v17, v17, 1.0
	v_rcp_f32_e32 v23, v20
	ds_read_b128 v[8:11], v186 offset:9312
	s_waitcnt lgkmcnt(2)
	v_mfma_f32_32x32x16_f16 v[82:97], v[4:7], v[138:141], v[82:97]
	v_div_fmas_f32 v4, v18, v19, v21
	v_div_fixup_f32 v176, v4, v16, -v41
	v_fma_f32 v4, -v20, v23, 1.0
	v_fmac_f32_e32 v23, v4, v23
	v_div_scale_f32 v4, vcc, 1.0, v17, 1.0
	v_mul_f32_e32 v5, v4, v23
	v_fma_f32 v6, -v20, v5, v4
	v_fmac_f32_e32 v5, v6, v23
	s_waitcnt lgkmcnt(1)
	v_mfma_f32_32x32x16_f16 v[66:81], v[12:15], v[126:129], v[66:81]
	v_fma_f32 v4, -v20, v5, v4
	v_div_fmas_f32 v4, v4, v23, v5
	v_div_fixup_f32 v177, v4, v17, 1.0
	v_mul_u32_u24_e32 v4, 0x90, v22
	v_add3_u32 v189, v40, v4, v2
	v_mul_u32_u24_e32 v2, 0x90, v1
	v_lshlrev_b32_e32 v4, 2, v99
	s_waitcnt lgkmcnt(0)
	v_mfma_f32_32x32x16_f16 v[82:97], v[8:11], v[142:145], v[82:97]
	v_add3_u32 v190, v40, v2, v4
	v_mul_u32_u24_e32 v2, 0x48, v1
	v_lshl_add_u32 v2, v2, 1, 0
	v_lshlrev_b32_e32 v4, 1, v101
	v_add3_u32 v191, v2, v4, v100
	s_mov_b32 s4, 0x3f800000
	s_mov_b32 s5, 0x10000
	v_mov_b32_e32 v2, v3
	v_mov_b32_e32 v4, v3
	v_mov_b32_e32 v5, v3
	v_mov_b32_e32 v6, v3
	v_mov_b32_e32 v7, v3
	v_mov_b32_e32 v8, v3
	v_mov_b32_e32 v9, v3
	v_mov_b32_e32 v10, v3
	v_mov_b32_e32 v11, v3
	v_mov_b32_e32 v12, v3
	v_mov_b32_e32 v13, v3
	v_mov_b32_e32 v14, v3
	v_mov_b32_e32 v15, v3
	v_mov_b32_e32 v16, v3
	v_mov_b32_e32 v17, v3
	v_mov_b32_e32 v18, v3
	v_mov_b32_e32 v19, v3
	v_mov_b32_e32 v20, v3
	v_mov_b32_e32 v21, v3
	v_mov_b32_e32 v22, v3
	v_mov_b32_e32 v23, v3
	v_mov_b32_e32 v28, v3
	v_mov_b32_e32 v29, v3
	v_mov_b32_e32 v30, v3
	v_mov_b32_e32 v31, v3
	v_mov_b32_e32 v32, v3
	v_mov_b32_e32 v33, v3
	v_mov_b32_e32 v34, v3
	v_mov_b32_e32 v35, v3
	v_mov_b32_e32 v36, v3
	v_mov_b32_e32 v37, v3
	v_mov_b32_e32 v38, v3
	v_mov_b32_e32 v39, v3
	v_mov_b32_e32 v40, v3
	v_mov_b32_e32 v41, v3
	v_mov_b32_e32 v42, v3
	v_mov_b32_e32 v43, v3
	v_mov_b32_e32 v44, v3
	v_mov_b32_e32 v45, v3
	v_mov_b32_e32 v46, v3
	v_mov_b32_e32 v47, v3
	v_mov_b32_e32 v48, v3
	v_mov_b32_e32 v49, v3
	v_mov_b32_e32 v50, v3
	v_mov_b32_e32 v51, v3
	v_mov_b32_e32 v52, v3
	v_mov_b32_e32 v53, v3
	v_mov_b32_e32 v54, v3
	v_mov_b32_e32 v56, v3
	v_mov_b32_e32 v57, v3
	v_mov_b32_e32 v58, v3
	v_mov_b32_e32 v59, v3
	v_mov_b32_e32 v60, v3
	v_mov_b32_e32 v61, v3
	v_mov_b32_e32 v62, v3
	v_mov_b32_e32 v63, v3
	v_mov_b32_e32 v64, v3
	v_mov_b32_e32 v65, v3
	v_add_u32_e32 v192, 0xd800, v191
	v_sub_f32_e32 v66, v66, v187
	v_sub_f32_e32 v67, v67, v187
	v_sub_f32_e32 v68, v68, v187
	v_sub_f32_e32 v69, v69, v187
	v_sub_f32_e32 v70, v70, v187
	v_sub_f32_e32 v71, v71, v187
	v_sub_f32_e32 v72, v72, v187
	v_sub_f32_e32 v73, v73, v187
	v_sub_f32_e32 v74, v74, v187
	v_sub_f32_e32 v75, v75, v187
	v_sub_f32_e32 v76, v76, v187
	v_sub_f32_e32 v77, v77, v187
	v_sub_f32_e32 v78, v78, v187
	v_sub_f32_e32 v79, v79, v187
	v_sub_f32_e32 v80, v80, v187
	v_sub_f32_e32 v81, v81, v187
	s_mov_b32 s27, 0x42c80000
	v_cmp_gt_f32_e64 vcc, |v188|, s27
	s_cbranch_vccnz .Ll2_gen
	v_sub_f32_e32 v238, 0, v188
	v_exp_f32_e32 v238, v238
	s_nop 0
	v_mul_f32_e32 v176, v176, v238
	s_barrier
	s_branch .Ll2f_top
